# non-leader waves prefetch next phase code into L2 by data loads while waiting in grid barrier
# speedup vs baseline: 1.0078x; 1.0060x over previous
.LBB0_2251:
	s_or_b64 exec, exec, s[2:3]
	s_branch .LBB0_2252
.Lpf_10:
	s_getpc_b64 s[4:5]
.Lpf_10_pc:
	s_add_u32 s4, s4, (.LBB0_3295-.Lpf_10_pc)&4294967295
	s_addc_u32 s5, s5, (.LBB0_3295-.Lpf_10_pc)>>32
	v_readlane_b32 s6, v254, 6
	s_lshr_b32 s7, s43, 3
	s_mul_i32 s7, s7, 7
	s_add_i32 s6, s6, s7
	s_add_i32 s6, s6, -1
	s_lshl_b32 s6, s6, 10
	s_min_u32 s6, s6, (.LBB0_3540-.LBB0_3295-1024)
	v_mbcnt_lo_u32_b32 v0, -1, 0
	v_mbcnt_hi_u32_b32 v0, -1, v0
	v_lshl_add_u32 v0, v0, 4, s6
	global_load_dwordx4 v[2:5], v0, s[4:5]
	s_waitcnt vmcnt(0)
